# down GEMM: non-scaled v_mfma_f32_16x16x128_f8f6f4 (unit scales were passed anyway) instead of the block-scale form; x0.5 back in the epilogue as in the baseline
# speedup vs baseline: 1.0066x; 1.0066x over previous
; #define PG8_STAGE(bufoff, gbase, voff) do { _Pragma("unroll") for (int _i = 0; _i < 2; ++_i) \
;         __builtin_amdgcn_global_load_lds((const unsigned*)((const char*)(gbase) + (voff)[_i]), (LAS unsigned*)(lds + (bufoff) + ldsw + _i * 8192), 16, 0, 0); } while (0)
; #define PG8_LDA(dst, b, h) do { _Pragma("unroll") for (int m = 0; m < 4; ++m) _Pragma("unroll") for (int k = 0; k < 2; ++k) dst[m][k] = *(const LAS bf16x8*)(lds + PG8_SA(b, h) + aoff + m * 2048 + k * KOFF); } while (0)
; #define PG8_LDB(dst, b, h) do { _Pragma("unroll") for (int n = 0; n < 2; ++n) _Pragma("unroll") for (int k = 0; k < 2; ++k) dst[n][k] = *(const LAS bf16x8*)(lds + PG8_SB(b, h) + boff + n * 2048 + k * KOFF); } while (0)
; #define PG8_WAIT_V(n) asm volatile("s_waitcnt vmcnt(" #n ")" ::: "memory")
; #define PG8_WAIT_L(n) asm volatile("s_waitcnt lgkmcnt(" #n ")" ::: "memory")
; #define PG8_BAR __builtin_amdgcn_s_barrier()
; #define PG8_SCHED __builtin_amdgcn_sched_barrier(0)
; #define PG8_AOFF(u_, o0, o1) do { _Pragma("unroll") for (int _i = 0; _i < 2; ++_i) { const int r0 = (u_).pm * BM + Rr[_i], r1 = r0 + HALF; \
;         const int g0 = GATHER ? g.rowidx[r0] : r0, g1 = GATHER ? g.rowidx[r1] : r1; \
;         o0[_i] = (unsigned)g0 * (unsigned)K + (unsigned)Cc[_i]; o1[_i] = (unsigned)g1 * (unsigned)K + (unsigned)Cc[_i]; } } while (0)
; template <class Epi, class Sched, bool GATHER, bool FP8 = false, bool ALIGN = true>
; __device__ __forceinline__ void gemm_phase(LAS unsigned char* lds, int wave, const Gemm g, const Sched& S, const Epi& E) {
;     ...
;             PG8_LDB(B0, 0, 0); PG8_LDB(B1, 0, 1); PG8_SCHED; PG8_LDA(At, 0, 0); PG8_STAGE(PG8_SA(1, 1), a1, ca1);
;             if (last && has_next) PG8_AOFF(nxt, ca0, ca1);
;             PG8_WAIT_V(8); PG8_WAIT_L(0); PG8_BAR; PG8_MMA(0, 0, At, B0); PG8_MMA(0, 1, At, B1); PG8_BAR; PG8_SCHED;
;             PG8_LDA(At, 0, 1); PG8_STAGE(PG8_SB(0, 0), b2, voffB0); PG8_STAGE(PG8_SB(0, 1), b2, voffB1); PG8_STAGE(PG8_SA(0, 0), a2, ca0);
;             PG8_WAIT_V(8); PG8_WAIT_L(0); PG8_BAR; PG8_MMA(1, 0, At, B0); PG8_MMA(1, 1, At, B1); PG8_BAR; PG8_SCHED;
;             PG8_LDB(B0, 1, 0); PG8_LDB(B1, 1, 1); PG8_SCHED; PG8_LDA(At, 1, 0); PG8_STAGE(PG8_SA(0, 1), a2, ca1);
.Lpeel_dn_b:
	s_xor_b64 s[50:51], s[84:85], -1
	s_add_u32 s14, s12, 0x100
	s_addc_u32 s15, s13, 0
	s_and_b64 s[12:13], s[80:81], exec
	s_cselect_b32 s13, s7, s15
	s_cselect_b32 s12, s6, s14
	s_add_u32 s14, s48, s82
	s_addc_u32 s15, s49, s83
	s_waitcnt vmcnt(8)
	s_add_u32 s79, s14, 0x100
	s_waitcnt lgkmcnt(0)
	s_addc_u32 s82, s15, 0
	s_and_b64 s[14:15], s[80:81], exec
	s_cselect_b32 s15, s5, s82
	s_cselect_b32 s14, s39, s79
	s_barrier
	s_setprio 1
	s_waitcnt lgkmcnt(0)
	v_mfma_f32_16x16x128_f8f6f4 v[188:191], v[16:23], v[56:63], 0
	v_mfma_f32_16x16x128_f8f6f4 v[184:187], v[24:31], v[56:63], 0
	v_mfma_f32_16x16x128_f8f6f4 v[172:175], v[16:23], v[48:55], 0
	v_mfma_f32_16x16x128_f8f6f4 v[168:171], v[24:31], v[48:55], 0
	v_mfma_f32_16x16x128_f8f6f4 v[156:159], v[16:23], v[40:47], 0
	v_mfma_f32_16x16x128_f8f6f4 v[152:155], v[24:31], v[40:47], 0
	v_mfma_f32_16x16x128_f8f6f4 v[140:143], v[16:23], v[32:39], 0
	v_mfma_f32_16x16x128_f8f6f4 v[136:139], v[24:31], v[32:39], 0
	s_setprio 0
	s_setprio 1
	v_mfma_f32_16x16x128_f8f6f4 v[180:183], v[0:7], v[56:63], 0
	v_mfma_f32_16x16x128_f8f6f4 v[176:179], v[8:15], v[56:63], 0
	v_mfma_f32_16x16x128_f8f6f4 v[164:167], v[0:7], v[48:55], 0
	v_mfma_f32_16x16x128_f8f6f4 v[160:163], v[8:15], v[48:55], 0
	v_mfma_f32_16x16x128_f8f6f4 v[148:151], v[0:7], v[40:47], 0
	v_mfma_f32_16x16x128_f8f6f4 v[144:147], v[8:15], v[40:47], 0
	v_mfma_f32_16x16x128_f8f6f4 v[132:135], v[0:7], v[32:39], 0
	v_mfma_f32_16x16x128_f8f6f4 v[128:131], v[8:15], v[32:39], 0
	s_setprio 0
	s_barrier
	s_mov_b32 m0, s34
	v_lshl_add_u64 v[196:197], s[14:15], 0, v[204:205]
	ds_read_b128 v[32:35], v240 offset:16384
	ds_read_b128 v[36:39], v240 offset:17408
	ds_read_b128 v[40:43], v240 offset:18432
	ds_read_b128 v[44:47], v240 offset:19456
	ds_read_b128 v[48:51], v240 offset:20480
	ds_read_b128 v[52:55], v240 offset:21504
	ds_read_b128 v[56:59], v240 offset:22528
	ds_read_b128 v[60:63], v240 offset:23552
	global_load_lds_dwordx4 v[196:197], off
	v_lshl_add_u64 v[198:199], s[14:15], 0, v[208:209]
	s_mov_b32 m0, s35
	v_lshl_add_u64 v[200:201], s[14:15], 0, v[206:207]
	global_load_lds_dwordx4 v[198:199], off
	s_mov_b32 m0, s40
	v_lshl_add_u64 v[202:203], s[14:15], 0, v[210:211]
	global_load_lds_dwordx4 v[200:201], off
	s_mov_b32 m0, s41
	v_mov_b32_e32 v213, v193
	global_load_lds_dwordx4 v[202:203], off
	s_mov_b32 m0, s31
	v_mov_b32_e32 v215, v193
	global_load_lds_dwordx4 v212, s[12:13]
	s_mov_b32 m0, s47
	v_lshl_add_u64 v[226:227], s[12:13], 0, v[212:213]
	global_load_lds_dwordx4 v214, s[12:13]
	s_waitcnt vmcnt(8)
	s_waitcnt lgkmcnt(0)
	v_lshl_add_u64 v[228:229], s[12:13], 0, v[214:215]
	s_barrier
	s_setprio 1
	s_waitcnt lgkmcnt(0)
	v_mfma_f32_16x16x128_f8f6f4 v[124:127], v[16:23], v[32:39], 0
	v_mfma_f32_16x16x128_f8f6f4 v[120:123], v[24:31], v[32:39], 0
	v_mfma_f32_16x16x128_f8f6f4 v[108:111], v[16:23], v[40:47], 0
	v_mfma_f32_16x16x128_f8f6f4 v[104:107], v[24:31], v[40:47], 0
	v_mfma_f32_16x16x128_f8f6f4 v[92:95], v[16:23], v[48:55], 0
	v_mfma_f32_16x16x128_f8f6f4 v[88:91], v[24:31], v[48:55], 0
	v_mfma_f32_16x16x128_f8f6f4 v[76:79], v[16:23], v[56:63], 0
	v_mfma_f32_16x16x128_f8f6f4 v[72:75], v[24:31], v[56:63], 0
	s_setprio 0
	s_setprio 1
	v_mfma_f32_16x16x128_f8f6f4 v[116:119], v[0:7], v[32:39], 0
	v_mfma_f32_16x16x128_f8f6f4 v[112:115], v[8:15], v[32:39], 0
	v_mfma_f32_16x16x128_f8f6f4 v[100:103], v[0:7], v[40:47], 0
	v_mfma_f32_16x16x128_f8f6f4 v[96:99], v[8:15], v[40:47], 0
	v_mfma_f32_16x16x128_f8f6f4 v[84:87], v[0:7], v[48:55], 0
	v_mfma_f32_16x16x128_f8f6f4 v[80:83], v[8:15], v[48:55], 0
	v_mfma_f32_16x16x128_f8f6f4 v[68:71], v[0:7], v[56:63], 0
	v_mfma_f32_16x16x128_f8f6f4 v[64:67], v[8:15], v[56:63], 0
	s_setprio 0
	s_barrier
	s_add_i32 s14, 0, 0x18000
	s_add_i32 s15, 0, 0x1c000
	v_add_u32_e32 v12, s14, v236
	v_add_u32_e32 v28, s15, v236
	ds_read_b128 v[0:3], v12
	ds_read_b128 v[4:7], v12 offset:1024
	ds_read_b128 v[8:11], v12 offset:2048
	ds_read_b128 v[12:15], v12 offset:3072
	ds_read_b128 v[16:19], v28
	ds_read_b128 v[20:23], v28 offset:1024
	ds_read_b128 v[24:27], v28 offset:2048
	ds_read_b128 v[28:31], v28 offset:3072
	s_mov_b32 m0, s53
	v_lshl_add_u64 v[224:225], s[12:13], 0, v[224:225]
	ds_read_b128 v[32:35], v240 offset:32768
	ds_read_b128 v[36:39], v240 offset:33792
	ds_read_b128 v[40:43], v240 offset:34816
	ds_read_b128 v[44:47], v240 offset:35840
	ds_read_b128 v[48:51], v240 offset:36864
	ds_read_b128 v[52:55], v240 offset:37888
	ds_read_b128 v[56:59], v240 offset:38912
	ds_read_b128 v[60:63], v240 offset:39936
	global_load_lds_dwordx4 v[224:225], off
	v_lshl_add_u64 v[222:223], s[12:13], 0, v[222:223]
	s_mov_b32 m0, s56
	s_nop 0
	global_load_lds_dwordx4 v[222:223], off
	s_waitcnt vmcnt(8)
	s_waitcnt lgkmcnt(0)
	s_barrier
; #define PG8_STAGE(bufoff, gbase, voff) do { _Pragma("unroll") for (int _i = 0; _i < 2; ++_i) \
;         __builtin_amdgcn_global_load_lds((const unsigned*)((const char*)(gbase) + (voff)[_i]), (LAS unsigned*)(lds + (bufoff) + ldsw + _i * 8192), 16, 0, 0); } while (0)
; #define PG8_LDA(dst, b, h) do { _Pragma("unroll") for (int m = 0; m < 4; ++m) _Pragma("unroll") for (int k = 0; k < 2; ++k) dst[m][k] = *(const LAS bf16x8*)(lds + PG8_SA(b, h) + aoff + m * 2048 + k * KOFF); } while (0)
; #define PG8_LDB(dst, b, h) do { _Pragma("unroll") for (int n = 0; n < 2; ++n) _Pragma("unroll") for (int k = 0; k < 2; ++k) dst[n][k] = *(const LAS bf16x8*)(lds + PG8_SB(b, h) + boff + n * 2048 + k * KOFF); } while (0)
; #define PG8_WAIT_V(n) asm volatile("s_waitcnt vmcnt(" #n ")" ::: "memory")
; #define PG8_WAIT_L(n) asm volatile("s_waitcnt lgkmcnt(" #n ")" ::: "memory")
; #define PG8_BAR __builtin_amdgcn_s_barrier()
; #define PG8_SCHED __builtin_amdgcn_sched_barrier(0)
; template <class Epi, class Sched, bool GATHER, bool FP8 = false, bool ALIGN = true>
; __device__ __forceinline__ void gemm_phase(LAS unsigned char* lds, int wave, const Gemm g, const Sched& S, const Epi& E) {
;     ...
;             PG8_LDB(B0, 1, 0); PG8_LDB(B1, 1, 1); PG8_SCHED; PG8_LDA(At, 1, 0); PG8_STAGE(PG8_SA(0, 1), a2, ca1);
;             PG8_WAIT_V(8); PG8_WAIT_L(0); PG8_BAR; PG8_MMA(0, 0, At, B0); PG8_MMA(0, 1, At, B1); PG8_BAR; PG8_SCHED;
;             PG8_LDA(At, 1, 1); PG8_STAGE(PG8_SB(1, 0), b3, voffB0); PG8_STAGE(PG8_SB(1, 1), b3, voffB1); PG8_STAGE(PG8_SA(1, 0), a3, ca0);
;             PG8_WAIT_V(8); PG8_WAIT_L(0); PG8_BAR; PG8_MMA(1, 0, At, B0); PG8_MMA(1, 1, At, B1); PG8_BAR; PG8_SCHED;
	s_setprio 1
	s_waitcnt lgkmcnt(0)
	v_mfma_f32_16x16x128_f8f6f4 v[188:191], v[0:7], v[32:39], v[188:191]
	v_mfma_f32_16x16x128_f8f6f4 v[184:187], v[8:15], v[32:39], v[184:187]
	v_mfma_f32_16x16x128_f8f6f4 v[172:175], v[0:7], v[40:47], v[172:175]
	v_mfma_f32_16x16x128_f8f6f4 v[168:171], v[8:15], v[40:47], v[168:171]
	v_mfma_f32_16x16x128_f8f6f4 v[156:159], v[0:7], v[48:55], v[156:159]
	v_mfma_f32_16x16x128_f8f6f4 v[152:155], v[8:15], v[48:55], v[152:155]
	v_mfma_f32_16x16x128_f8f6f4 v[140:143], v[0:7], v[56:63], v[140:143]
	v_mfma_f32_16x16x128_f8f6f4 v[136:139], v[8:15], v[56:63], v[136:139]
	s_setprio 0
	s_setprio 1
	v_mfma_f32_16x16x128_f8f6f4 v[180:183], v[16:23], v[32:39], v[180:183]
	v_mfma_f32_16x16x128_f8f6f4 v[176:179], v[24:31], v[32:39], v[176:179]
	v_mfma_f32_16x16x128_f8f6f4 v[164:167], v[16:23], v[40:47], v[164:167]
	v_mfma_f32_16x16x128_f8f6f4 v[160:163], v[24:31], v[40:47], v[160:163]
	v_mfma_f32_16x16x128_f8f6f4 v[148:151], v[16:23], v[48:55], v[148:151]
	v_mfma_f32_16x16x128_f8f6f4 v[144:147], v[24:31], v[48:55], v[144:147]
	v_mfma_f32_16x16x128_f8f6f4 v[132:135], v[16:23], v[56:63], v[132:135]
	v_mfma_f32_16x16x128_f8f6f4 v[128:131], v[24:31], v[56:63], v[128:131]
	s_setprio 0
	s_barrier
	s_add_i32 s12, s14, s30
	v_lshl_add_u64 v[196:197], v[196:197], 0, s[62:63]
	s_mov_b32 m0, s12
	ds_read_b128 v[32:35], v240 offset:49152
	ds_read_b128 v[36:39], v240 offset:50176
	ds_read_b128 v[40:43], v240 offset:51200
	ds_read_b128 v[44:47], v240 offset:52224
	ds_read_b128 v[48:51], v240 offset:53248
	ds_read_b128 v[52:55], v240 offset:54272
	ds_read_b128 v[56:59], v240 offset:55296
	ds_read_b128 v[60:63], v240 offset:56320
	global_load_lds_dwordx4 v[196:197], off
	v_lshl_add_u64 v[196:197], v[198:199], 0, s[62:63]
	s_add_i32 m0, s12, 0x2000
	s_add_i32 s12, s15, s30
	global_load_lds_dwordx4 v[196:197], off
	v_lshl_add_u64 v[196:197], v[200:201], 0, s[62:63]
	s_mov_b32 m0, s12
	s_nop 0
	global_load_lds_dwordx4 v[196:197], off
	v_lshl_add_u64 v[196:197], v[202:203], 0, s[62:63]
	s_add_i32 m0, s12, 0x2000
	s_nop 0
	global_load_lds_dwordx4 v[196:197], off
	v_lshl_add_u64 v[196:197], v[226:227], 0, s[62:63]
	s_mov_b32 m0, s57
	s_nop 0
	global_load_lds_dwordx4 v[196:197], off
	v_lshl_add_u64 v[196:197], v[228:229], 0, s[62:63]
	s_mov_b32 m0, s58
	s_nop 0
	global_load_lds_dwordx4 v[196:197], off
	s_waitcnt vmcnt(8)
	s_waitcnt lgkmcnt(0)
	s_barrier
	s_setprio 1
	s_waitcnt lgkmcnt(0)
	v_mfma_f32_16x16x128_f8f6f4 v[124:127], v[0:7], v[32:39], v[124:127]
	v_mfma_f32_16x16x128_f8f6f4 v[120:123], v[8:15], v[32:39], v[120:123]
	v_mfma_f32_16x16x128_f8f6f4 v[108:111], v[0:7], v[40:47], v[108:111]
	v_mfma_f32_16x16x128_f8f6f4 v[104:107], v[8:15], v[40:47], v[104:107]
	v_mfma_f32_16x16x128_f8f6f4 v[92:95], v[0:7], v[48:55], v[92:95]
	v_mfma_f32_16x16x128_f8f6f4 v[88:91], v[8:15], v[48:55], v[88:91]
	v_mfma_f32_16x16x128_f8f6f4 v[76:79], v[0:7], v[56:63], v[76:79]
	v_mfma_f32_16x16x128_f8f6f4 v[72:75], v[8:15], v[56:63], v[72:75]
	s_setprio 0
	s_setprio 1
	v_mfma_f32_16x16x128_f8f6f4 v[116:119], v[16:23], v[32:39], v[116:119]
	v_mfma_f32_16x16x128_f8f6f4 v[112:115], v[24:31], v[32:39], v[112:115]
	v_mfma_f32_16x16x128_f8f6f4 v[100:103], v[16:23], v[40:47], v[100:103]
	v_mfma_f32_16x16x128_f8f6f4 v[96:99], v[24:31], v[40:47], v[96:99]
	v_mfma_f32_16x16x128_f8f6f4 v[84:87], v[16:23], v[48:55], v[84:87]
	v_mfma_f32_16x16x128_f8f6f4 v[80:83], v[24:31], v[48:55], v[80:83]
	v_mfma_f32_16x16x128_f8f6f4 v[68:71], v[16:23], v[56:63], v[68:71]
	v_mfma_f32_16x16x128_f8f6f4 v[64:67], v[24:31], v[56:63], v[64:67]
	s_setprio 0
	s_barrier
	s_mov_b64 s[84:85], 0
	s_mov_b64 s[80:81], -1
	s_and_b64 vcc, exec, s[50:51]
	s_cbranch_vccnz .LBB0_1160
	s_mov_b64 s[82:83], 0x100
	s_branch .LBB0_1155

; #define PG8_STAGE(bufoff, gbase, voff) do { _Pragma("unroll") for (int _i = 0; _i < 2; ++_i) \
;         __builtin_amdgcn_global_load_lds((const unsigned*)((const char*)(gbase) + (voff)[_i]), (LAS unsigned*)(lds + (bufoff) + ldsw + _i * 8192), 16, 0, 0); } while (0)
; #define PG8_LDA(dst, b, h) do { _Pragma("unroll") for (int m = 0; m < 4; ++m) _Pragma("unroll") for (int k = 0; k < 2; ++k) dst[m][k] = *(const LAS bf16x8*)(lds + PG8_SA(b, h) + aoff + m * 2048 + k * KOFF); } while (0)
; #define PG8_LDB(dst, b, h) do { _Pragma("unroll") for (int n = 0; n < 2; ++n) _Pragma("unroll") for (int k = 0; k < 2; ++k) dst[n][k] = *(const LAS bf16x8*)(lds + PG8_SB(b, h) + boff + n * 2048 + k * KOFF); } while (0)
; #define PG8_WAIT_V(n) asm volatile("s_waitcnt vmcnt(" #n ")" ::: "memory")
; #define PG8_WAIT_L(n) asm volatile("s_waitcnt lgkmcnt(" #n ")" ::: "memory")
; #define PG8_BAR __builtin_amdgcn_s_barrier()
; #define PG8_SCHED __builtin_amdgcn_sched_barrier(0)
; #define PG8_AOFF(u_, o0, o1) do { _Pragma("unroll") for (int _i = 0; _i < 2; ++_i) { const int r0 = (u_).pm * BM + Rr[_i], r1 = r0 + HALF; \
;         const int g0 = GATHER ? g.rowidx[r0] : r0, g1 = GATHER ? g.rowidx[r1] : r1; \
;         o0[_i] = (unsigned)g0 * (unsigned)K + (unsigned)Cc[_i]; o1[_i] = (unsigned)g1 * (unsigned)K + (unsigned)Cc[_i]; } } while (0)
; template <class Epi, class Sched, bool GATHER, bool FP8 = false, bool ALIGN = true>
; __device__ __forceinline__ void gemm_phase(LAS unsigned char* lds, int wave, const Gemm g, const Sched& S, const Epi& E) {
;     ...
;             PG8_LDB(B0, 0, 0); PG8_LDB(B1, 0, 1); PG8_SCHED; PG8_LDA(At, 0, 0); PG8_STAGE(PG8_SA(1, 1), a1, ca1);
;             if (last && has_next) PG8_AOFF(nxt, ca0, ca1);
;             PG8_WAIT_V(8); PG8_WAIT_L(0); PG8_BAR; PG8_MMA(0, 0, At, B0); PG8_MMA(0, 1, At, B1); PG8_BAR; PG8_SCHED;
;             PG8_LDA(At, 0, 1); PG8_STAGE(PG8_SB(0, 0), b2, voffB0); PG8_STAGE(PG8_SB(0, 1), b2, voffB1); PG8_STAGE(PG8_SA(0, 0), a2, ca0);
;             PG8_WAIT_V(8); PG8_WAIT_L(0); PG8_BAR; PG8_MMA(1, 0, At, B0); PG8_MMA(1, 1, At, B1); PG8_BAR; PG8_SCHED;
.LBB0_1158:
	s_xor_b64 s[50:51], s[84:85], -1
	s_add_u32 s14, s12, 0x100
	s_addc_u32 s15, s13, 0
	s_and_b64 s[12:13], s[80:81], exec
	s_cselect_b32 s13, s7, s15
	s_cselect_b32 s12, s6, s14
	s_add_u32 s14, s48, s82
	s_addc_u32 s15, s49, s83
	s_waitcnt vmcnt(8)
	s_add_u32 s79, s14, 0x100
	s_waitcnt lgkmcnt(0)
	s_addc_u32 s82, s15, 0
	s_and_b64 s[14:15], s[80:81], exec
	s_cselect_b32 s15, s5, s82
	s_cselect_b32 s14, s39, s79
	s_barrier
	s_setprio 1
	s_waitcnt lgkmcnt(0)
	v_mfma_f32_16x16x128_f8f6f4 v[188:191], v[16:23], v[56:63], v[188:191]
	v_mfma_f32_16x16x128_f8f6f4 v[184:187], v[24:31], v[56:63], v[184:187]
	v_mfma_f32_16x16x128_f8f6f4 v[172:175], v[16:23], v[48:55], v[172:175]
	v_mfma_f32_16x16x128_f8f6f4 v[168:171], v[24:31], v[48:55], v[168:171]
	v_mfma_f32_16x16x128_f8f6f4 v[156:159], v[16:23], v[40:47], v[156:159]
	v_mfma_f32_16x16x128_f8f6f4 v[152:155], v[24:31], v[40:47], v[152:155]
	v_mfma_f32_16x16x128_f8f6f4 v[140:143], v[16:23], v[32:39], v[140:143]
	v_mfma_f32_16x16x128_f8f6f4 v[136:139], v[24:31], v[32:39], v[136:139]
	s_setprio 0
	s_setprio 1
	v_mfma_f32_16x16x128_f8f6f4 v[180:183], v[0:7], v[56:63], v[180:183]
	v_mfma_f32_16x16x128_f8f6f4 v[176:179], v[8:15], v[56:63], v[176:179]
	v_mfma_f32_16x16x128_f8f6f4 v[164:167], v[0:7], v[48:55], v[164:167]
	v_mfma_f32_16x16x128_f8f6f4 v[160:163], v[8:15], v[48:55], v[160:163]
	v_mfma_f32_16x16x128_f8f6f4 v[148:151], v[0:7], v[40:47], v[148:151]
	v_mfma_f32_16x16x128_f8f6f4 v[144:147], v[8:15], v[40:47], v[144:147]
	v_mfma_f32_16x16x128_f8f6f4 v[132:135], v[0:7], v[32:39], v[132:135]
	v_mfma_f32_16x16x128_f8f6f4 v[128:131], v[8:15], v[32:39], v[128:131]
	s_setprio 0
	s_barrier
	s_mov_b32 m0, s34
	v_lshl_add_u64 v[196:197], s[14:15], 0, v[204:205]
	ds_read_b128 v[32:35], v240 offset:16384
	ds_read_b128 v[36:39], v240 offset:17408
	ds_read_b128 v[40:43], v240 offset:18432
	ds_read_b128 v[44:47], v240 offset:19456
	ds_read_b128 v[48:51], v240 offset:20480
	ds_read_b128 v[52:55], v240 offset:21504
	ds_read_b128 v[56:59], v240 offset:22528
	ds_read_b128 v[60:63], v240 offset:23552
	global_load_lds_dwordx4 v[196:197], off
	v_lshl_add_u64 v[198:199], s[14:15], 0, v[208:209]
	s_mov_b32 m0, s35
	v_lshl_add_u64 v[200:201], s[14:15], 0, v[206:207]
	global_load_lds_dwordx4 v[198:199], off
	s_mov_b32 m0, s40
	v_lshl_add_u64 v[202:203], s[14:15], 0, v[210:211]
	global_load_lds_dwordx4 v[200:201], off
	s_mov_b32 m0, s41
	v_mov_b32_e32 v213, v193
	global_load_lds_dwordx4 v[202:203], off
	s_mov_b32 m0, s31
	v_mov_b32_e32 v215, v193
	global_load_lds_dwordx4 v212, s[12:13]
	s_mov_b32 m0, s47
	v_lshl_add_u64 v[226:227], s[12:13], 0, v[212:213]
	global_load_lds_dwordx4 v214, s[12:13]
	s_waitcnt vmcnt(8)
	s_waitcnt lgkmcnt(0)
	v_lshl_add_u64 v[228:229], s[12:13], 0, v[214:215]
	s_barrier
	s_setprio 1
	s_waitcnt lgkmcnt(0)
	v_mfma_f32_16x16x128_f8f6f4 v[124:127], v[16:23], v[32:39], v[124:127]
	v_mfma_f32_16x16x128_f8f6f4 v[120:123], v[24:31], v[32:39], v[120:123]
	v_mfma_f32_16x16x128_f8f6f4 v[108:111], v[16:23], v[40:47], v[108:111]
	v_mfma_f32_16x16x128_f8f6f4 v[104:107], v[24:31], v[40:47], v[104:107]
	v_mfma_f32_16x16x128_f8f6f4 v[92:95], v[16:23], v[48:55], v[92:95]
	v_mfma_f32_16x16x128_f8f6f4 v[88:91], v[24:31], v[48:55], v[88:91]
	v_mfma_f32_16x16x128_f8f6f4 v[76:79], v[16:23], v[56:63], v[76:79]
	v_mfma_f32_16x16x128_f8f6f4 v[72:75], v[24:31], v[56:63], v[72:75]
	s_setprio 0
	s_setprio 1
	v_mfma_f32_16x16x128_f8f6f4 v[116:119], v[0:7], v[32:39], v[116:119]
	v_mfma_f32_16x16x128_f8f6f4 v[112:115], v[8:15], v[32:39], v[112:115]
	v_mfma_f32_16x16x128_f8f6f4 v[100:103], v[0:7], v[40:47], v[100:103]
	v_mfma_f32_16x16x128_f8f6f4 v[96:99], v[8:15], v[40:47], v[96:99]
	v_mfma_f32_16x16x128_f8f6f4 v[84:87], v[0:7], v[48:55], v[84:87]
	v_mfma_f32_16x16x128_f8f6f4 v[80:83], v[8:15], v[48:55], v[80:83]
	v_mfma_f32_16x16x128_f8f6f4 v[68:71], v[0:7], v[56:63], v[68:71]
	v_mfma_f32_16x16x128_f8f6f4 v[64:67], v[8:15], v[56:63], v[64:67]
	s_setprio 0
	s_barrier
; #define PG8_STAGE(bufoff, gbase, voff) do { _Pragma("unroll") for (int _i = 0; _i < 2; ++_i) \
;         __builtin_amdgcn_global_load_lds((const unsigned*)((const char*)(gbase) + (voff)[_i]), (LAS unsigned*)(lds + (bufoff) + ldsw + _i * 8192), 16, 0, 0); } while (0)
; #define PG8_LDA(dst, b, h) do { _Pragma("unroll") for (int m = 0; m < 4; ++m) _Pragma("unroll") for (int k = 0; k < 2; ++k) dst[m][k] = *(const LAS bf16x8*)(lds + PG8_SA(b, h) + aoff + m * 2048 + k * KOFF); } while (0)
; #define PG8_LDB(dst, b, h) do { _Pragma("unroll") for (int n = 0; n < 2; ++n) _Pragma("unroll") for (int k = 0; k < 2; ++k) dst[n][k] = *(const LAS bf16x8*)(lds + PG8_SB(b, h) + boff + n * 2048 + k * KOFF); } while (0)
; #define PG8_WAIT_V(n) asm volatile("s_waitcnt vmcnt(" #n ")" ::: "memory")
; #define PG8_WAIT_L(n) asm volatile("s_waitcnt lgkmcnt(" #n ")" ::: "memory")
; #define PG8_BAR __builtin_amdgcn_s_barrier()
; #define PG8_SCHED __builtin_amdgcn_sched_barrier(0)
; template <class Epi, class Sched, bool GATHER, bool FP8 = false, bool ALIGN = true>
; __device__ __forceinline__ void gemm_phase(LAS unsigned char* lds, int wave, const Gemm g, const Sched& S, const Epi& E) {
;     ...
;             PG8_LDB(B0, 1, 0); PG8_LDB(B1, 1, 1); PG8_SCHED; PG8_LDA(At, 1, 0); PG8_STAGE(PG8_SA(0, 1), a2, ca1);
;             PG8_WAIT_V(8); PG8_WAIT_L(0); PG8_BAR; PG8_MMA(0, 0, At, B0); PG8_MMA(0, 1, At, B1); PG8_BAR; PG8_SCHED;
;             PG8_LDA(At, 1, 1); PG8_STAGE(PG8_SB(1, 0), b3, voffB0); PG8_STAGE(PG8_SB(1, 1), b3, voffB1); PG8_STAGE(PG8_SA(1, 0), a3, ca0);
;             PG8_WAIT_V(8); PG8_WAIT_L(0); PG8_BAR; PG8_MMA(1, 0, At, B0); PG8_MMA(1, 1, At, B1); PG8_BAR; PG8_SCHED;
	s_add_i32 s14, 0, 0x18000
	s_add_i32 s15, 0, 0x1c000
	v_add_u32_e32 v12, s14, v236
	v_add_u32_e32 v28, s15, v236
	ds_read_b128 v[0:3], v12
	ds_read_b128 v[4:7], v12 offset:1024
	ds_read_b128 v[8:11], v12 offset:2048
	ds_read_b128 v[12:15], v12 offset:3072
	ds_read_b128 v[16:19], v28
	ds_read_b128 v[20:23], v28 offset:1024
	ds_read_b128 v[24:27], v28 offset:2048
	ds_read_b128 v[28:31], v28 offset:3072
	s_mov_b32 m0, s53
	v_lshl_add_u64 v[224:225], s[12:13], 0, v[224:225]
	ds_read_b128 v[32:35], v240 offset:32768
	ds_read_b128 v[36:39], v240 offset:33792
	ds_read_b128 v[40:43], v240 offset:34816
	ds_read_b128 v[44:47], v240 offset:35840
	ds_read_b128 v[48:51], v240 offset:36864
	ds_read_b128 v[52:55], v240 offset:37888
	ds_read_b128 v[56:59], v240 offset:38912
	ds_read_b128 v[60:63], v240 offset:39936
	global_load_lds_dwordx4 v[224:225], off
	v_lshl_add_u64 v[222:223], s[12:13], 0, v[222:223]
	s_mov_b32 m0, s56
	s_nop 0
	global_load_lds_dwordx4 v[222:223], off
	s_waitcnt vmcnt(8)
	s_waitcnt lgkmcnt(0)
	s_barrier
	s_setprio 1
	s_waitcnt lgkmcnt(0)
	v_mfma_f32_16x16x128_f8f6f4 v[188:191], v[0:7], v[32:39], v[188:191]
	v_mfma_f32_16x16x128_f8f6f4 v[184:187], v[8:15], v[32:39], v[184:187]
	v_mfma_f32_16x16x128_f8f6f4 v[172:175], v[0:7], v[40:47], v[172:175]
	v_mfma_f32_16x16x128_f8f6f4 v[168:171], v[8:15], v[40:47], v[168:171]
	v_mfma_f32_16x16x128_f8f6f4 v[156:159], v[0:7], v[48:55], v[156:159]
	v_mfma_f32_16x16x128_f8f6f4 v[152:155], v[8:15], v[48:55], v[152:155]
	v_mfma_f32_16x16x128_f8f6f4 v[140:143], v[0:7], v[56:63], v[140:143]
	v_mfma_f32_16x16x128_f8f6f4 v[136:139], v[8:15], v[56:63], v[136:139]
	s_setprio 0
	s_setprio 1
	v_mfma_f32_16x16x128_f8f6f4 v[180:183], v[16:23], v[32:39], v[180:183]
	v_mfma_f32_16x16x128_f8f6f4 v[176:179], v[24:31], v[32:39], v[176:179]
	v_mfma_f32_16x16x128_f8f6f4 v[164:167], v[16:23], v[40:47], v[164:167]
	v_mfma_f32_16x16x128_f8f6f4 v[160:163], v[24:31], v[40:47], v[160:163]
	v_mfma_f32_16x16x128_f8f6f4 v[148:151], v[16:23], v[48:55], v[148:151]
	v_mfma_f32_16x16x128_f8f6f4 v[144:147], v[24:31], v[48:55], v[144:147]
	v_mfma_f32_16x16x128_f8f6f4 v[132:135], v[16:23], v[56:63], v[132:135]
	v_mfma_f32_16x16x128_f8f6f4 v[128:131], v[24:31], v[56:63], v[128:131]
	s_setprio 0
	s_barrier
	s_add_i32 s12, s14, s30
	v_lshl_add_u64 v[196:197], v[196:197], 0, s[62:63]
	s_mov_b32 m0, s12
	ds_read_b128 v[32:35], v240 offset:49152
	ds_read_b128 v[36:39], v240 offset:50176
	ds_read_b128 v[40:43], v240 offset:51200
	ds_read_b128 v[44:47], v240 offset:52224
	ds_read_b128 v[48:51], v240 offset:53248
	ds_read_b128 v[52:55], v240 offset:54272
	ds_read_b128 v[56:59], v240 offset:55296
	ds_read_b128 v[60:63], v240 offset:56320
	global_load_lds_dwordx4 v[196:197], off
	v_lshl_add_u64 v[196:197], v[198:199], 0, s[62:63]
	s_add_i32 m0, s12, 0x2000
	s_add_i32 s12, s15, s30
	global_load_lds_dwordx4 v[196:197], off
	v_lshl_add_u64 v[196:197], v[200:201], 0, s[62:63]
	s_mov_b32 m0, s12
	s_nop 0
	global_load_lds_dwordx4 v[196:197], off
	v_lshl_add_u64 v[196:197], v[202:203], 0, s[62:63]
	s_add_i32 m0, s12, 0x2000
	s_nop 0
	global_load_lds_dwordx4 v[196:197], off
	v_lshl_add_u64 v[196:197], v[226:227], 0, s[62:63]
	s_mov_b32 m0, s57
	s_nop 0
	global_load_lds_dwordx4 v[196:197], off
	v_lshl_add_u64 v[196:197], v[228:229], 0, s[62:63]
	s_mov_b32 m0, s58
	s_nop 0
	global_load_lds_dwordx4 v[196:197], off
	s_waitcnt vmcnt(8)
	s_waitcnt lgkmcnt(0)
	s_barrier
	s_setprio 1
	s_waitcnt lgkmcnt(0)
	v_mfma_f32_16x16x128_f8f6f4 v[124:127], v[0:7], v[32:39], v[124:127]
	v_mfma_f32_16x16x128_f8f6f4 v[120:123], v[8:15], v[32:39], v[120:123]
	v_mfma_f32_16x16x128_f8f6f4 v[108:111], v[0:7], v[40:47], v[108:111]
	v_mfma_f32_16x16x128_f8f6f4 v[104:107], v[8:15], v[40:47], v[104:107]
	v_mfma_f32_16x16x128_f8f6f4 v[92:95], v[0:7], v[48:55], v[92:95]
	v_mfma_f32_16x16x128_f8f6f4 v[88:91], v[8:15], v[48:55], v[88:91]
	v_mfma_f32_16x16x128_f8f6f4 v[76:79], v[0:7], v[56:63], v[76:79]
	v_mfma_f32_16x16x128_f8f6f4 v[72:75], v[8:15], v[56:63], v[72:75]
	s_setprio 0
	s_setprio 1
	v_mfma_f32_16x16x128_f8f6f4 v[116:119], v[16:23], v[32:39], v[116:119]
	v_mfma_f32_16x16x128_f8f6f4 v[112:115], v[24:31], v[32:39], v[112:115]
	v_mfma_f32_16x16x128_f8f6f4 v[100:103], v[16:23], v[40:47], v[100:103]
	v_mfma_f32_16x16x128_f8f6f4 v[96:99], v[24:31], v[40:47], v[96:99]
	v_mfma_f32_16x16x128_f8f6f4 v[84:87], v[16:23], v[48:55], v[84:87]
	v_mfma_f32_16x16x128_f8f6f4 v[80:83], v[24:31], v[48:55], v[80:83]
	v_mfma_f32_16x16x128_f8f6f4 v[68:71], v[16:23], v[56:63], v[68:71]
	v_mfma_f32_16x16x128_f8f6f4 v[64:67], v[24:31], v[56:63], v[64:67]
	s_setprio 0
	s_barrier
	s_mov_b64 s[84:85], 0
	s_mov_b64 s[80:81], -1
	s_and_b64 vcc, exec, s[50:51]
	s_cbranch_vccnz .LBB0_1160
	s_mov_b64 s[82:83], 0x100
	s_branch .LBB0_1155
